# attention unit prologue: KMAX bound loads also issued with the Q loads, on top of v9_prohoist
# baseline (speedup 1.0000x reference)
.LBB0_1115:
	v_add_u32_e32 v4, s3, v191
	v_ashrrev_i32_e32 v5, 31, v4
	s_and_saveexec_b64 s[0:1], s[38:39]
	s_xor_b64 s[0:1], exec, s[0:1]
	v_lshlrev_b64 v[4:5], 6, v[4:5]
	s_movk_i32 s24, 0xff80
	v_lshl_add_u64 v[4:5], v[182:183], 0, v[4:5]
	s_mov_b32 s25, -1
	v_lshl_add_u64 v[8:9], v[4:5], 0, s[24:25]
	s_or_saveexec_b64 s[0:1], s[0:1]
	s_and_b32 s35, s15, 7
	s_xor_b64 exec, exec, s[0:1]
	v_lshlrev_b64 v[4:5], 10, v[4:5]
	v_lshl_add_u64 v[4:5], s[48:49], 0, v[4:5]
	s_lshl_b32 s30, s35, 7
	v_lshl_add_u64 v[4:5], v[4:5], 0, s[30:31]
	v_lshl_add_u64 v[8:9], v[184:185], 1, v[4:5]
	s_or_b64 exec, exec, s[0:1]
	v_add_u32_e32 v4, s3, v193
	v_ashrrev_i32_e32 v5, 31, v4
	s_and_saveexec_b64 s[0:1], s[40:41]
	s_xor_b64 s[0:1], exec, s[0:1]
	v_lshlrev_b64 v[4:5], 6, v[4:5]
	s_movk_i32 s24, 0xff80
	v_lshl_add_u64 v[4:5], v[186:187], 0, v[4:5]
	s_mov_b32 s25, -1
	v_lshl_add_u64 v[10:11], v[4:5], 0, s[24:25]
	s_or_saveexec_b64 s[0:1], s[0:1]
	v_mov_b32_e32 v199, 0x1000
	s_xor_b64 exec, exec, s[0:1]
	v_lshlrev_b64 v[4:5], 10, v[4:5]
	v_lshl_add_u64 v[4:5], s[48:49], 0, v[4:5]
	s_lshl_b32 s30, s35, 7
	v_lshl_add_u64 v[4:5], v[4:5], 0, s[30:31]
	v_lshl_add_u64 v[10:11], v[188:189], 1, v[4:5]
	v_mov_b32_e32 v199, 0x10000
	s_or_b64 exec, exec, s[0:1]
	v_add_u32_e32 v200, s7, v214
	v_mov_b64_e32 v[4:5], s[46:47]
	s_movk_i32 s0, 0x600
	v_mad_i64_i32 v[4:5], s[0:1], v200, s0, v[4:5]
	s_mul_i32 s30, s35, 0xc0
	v_lshl_add_u64 v[4:5], v[4:5], 0, s[30:31]
	v_lshl_add_u64 v[4:5], v[4:5], 0, v[2:3]
	global_load_dwordx4 v[132:135], v[4:5], off
	global_load_dwordx4 v[136:139], v[4:5], off offset:32
	global_load_dwordx4 v[140:143], v[4:5], off offset:64
	global_load_dwordx4 v[144:147], v[4:5], off offset:96
	global_load_dwordx4 v[148:151], v[4:5], off offset:128
	global_load_dwordx4 v[152:155], v[4:5], off offset:160
	s_lshl_b32 s0, s2, 3
	s_or_b32 s0, s0, s35
	v_lshl_add_u32 v156, s0, 6, v203
	v_lshl_add_u32 v160, v190, 1, v10
	v_mad_u64_u32 v[158:159], vcc, v156, s28, v[192:193]
	v_subrev_u32_e32 v160, s44, v160
	v_subrev_u32_e32 v161, s44, v8
	s_or_b32 s0, s23, 1
	s_sub_i32 s1, s0, s34
	s_min_u32 s0, s0, s1
	v_mad_i32_i24 v162, v199, s23, v160
	v_lshl_add_u32 v163, s23, 7, v158
	v_lshl_add_u32 v164, s23, v215, v161
	v_lshl_add_u32 v165, s0, v215, v161
	v_mad_i32_i24 v156, v199, s0, v160
	global_load_dwordx2 v[120:121], v162, s[44:45]
	global_load_dwordx4 v[122:125], v163, s[44:45]
	global_load_dwordx4 v[116:119], v164, s[44:45]
	global_load_dwordx4 v[126:129], v165, s[44:45]
	global_load_dwordx2 v[130:131], v156, s[44:45]
	s_lshl_b32 s0, s2, 3
	s_or_b32 s0, s0, s35
	s_ashr_i32 s1, s0, 31
	s_lshl_b64 s[0:1], s[0:1], 2
	s_add_u32 s0, s21, s0
	s_addc_u32 s1, s22, s1
	global_load_dword v157, v3, s[0:1]
	s_mov_b32 s0, s2
	s_ashr_i32 s1, s2, 31
	s_lshl_b64 s[0:1], s[0:1], 2
	s_add_u32 s0, s21, s0
	s_addc_u32 s1, s22, s1
	global_load_dword v166, v3, s[0:1] offset:256
	s_andn2_b64 vcc, exec, s[12:13]
	s_mov_b64 s[0:1], -1
	s_cbranch_vccnz .LBB0_1125
	s_mov_b64 s[0:1], 0

.LBB0_1127:
	s_lshl_b32 s0, s2, 3
	s_or_b32 s0, s0, s35
	v_lshl_add_u32 v5, s0, 6, v203
	v_lshl_add_u32 v4, v190, 1, v10
	v_mad_u64_u32 v[204:205], s[12:13], v5, s28, v[192:193]
	s_waitcnt vmcnt(0)
	v_and_b32_e32 v5, 0xffff0000, v132
	v_subrev_u32_e32 v202, s44, v4
	v_lshlrev_b32_e32 v4, 16, v132
	v_mul_f32_e32 v6, v5, v5
	v_fmac_f32_e32 v6, v4, v4
	v_lshlrev_b32_e32 v4, 16, v133
	v_fmac_f32_e32 v6, v4, v4
	v_and_b32_e32 v4, 0xffff0000, v133
	v_fmac_f32_e32 v6, v4, v4
	v_lshlrev_b32_e32 v4, 16, v134
	v_fmac_f32_e32 v6, v4, v4
	v_and_b32_e32 v4, 0xffff0000, v134
	v_fmac_f32_e32 v6, v4, v4
	v_lshlrev_b32_e32 v4, 16, v135
	v_fmac_f32_e32 v6, v4, v4
	v_and_b32_e32 v4, 0xffff0000, v135
	v_fmac_f32_e32 v6, v4, v4
	v_lshlrev_b32_e32 v4, 16, v136
	v_fmac_f32_e32 v6, v4, v4
	v_and_b32_e32 v4, 0xffff0000, v136
	v_fmac_f32_e32 v6, v4, v4
	v_lshlrev_b32_e32 v4, 16, v137
	v_fmac_f32_e32 v6, v4, v4
	v_and_b32_e32 v4, 0xffff0000, v137
	v_fmac_f32_e32 v6, v4, v4
	v_lshlrev_b32_e32 v4, 16, v138
	v_fmac_f32_e32 v6, v4, v4
	v_and_b32_e32 v4, 0xffff0000, v138
	v_fmac_f32_e32 v6, v4, v4
	v_lshlrev_b32_e32 v4, 16, v139
	v_fmac_f32_e32 v6, v4, v4
	v_and_b32_e32 v4, 0xffff0000, v139
	v_fmac_f32_e32 v6, v4, v4
	v_lshlrev_b32_e32 v4, 16, v140
	v_fmac_f32_e32 v6, v4, v4
	v_and_b32_e32 v4, 0xffff0000, v140
	v_fmac_f32_e32 v6, v4, v4
	v_lshlrev_b32_e32 v4, 16, v141
	v_fmac_f32_e32 v6, v4, v4
	v_and_b32_e32 v4, 0xffff0000, v141
	v_fmac_f32_e32 v6, v4, v4
	v_lshlrev_b32_e32 v4, 16, v142
	v_fmac_f32_e32 v6, v4, v4
	v_and_b32_e32 v4, 0xffff0000, v142
	v_fmac_f32_e32 v6, v4, v4
	v_lshlrev_b32_e32 v4, 16, v143
	v_fmac_f32_e32 v6, v4, v4
	v_and_b32_e32 v4, 0xffff0000, v143
	v_fmac_f32_e32 v6, v4, v4
	v_lshlrev_b32_e32 v4, 16, v144
	v_fmac_f32_e32 v6, v4, v4
	v_and_b32_e32 v4, 0xffff0000, v144
	v_fmac_f32_e32 v6, v4, v4
	v_lshlrev_b32_e32 v4, 16, v145
	v_fmac_f32_e32 v6, v4, v4
	v_and_b32_e32 v4, 0xffff0000, v145
	v_fmac_f32_e32 v6, v4, v4
	v_lshlrev_b32_e32 v4, 16, v146
	v_fmac_f32_e32 v6, v4, v4
	v_and_b32_e32 v4, 0xffff0000, v146
	v_fmac_f32_e32 v6, v4, v4
	v_lshlrev_b32_e32 v4, 16, v147
	v_fmac_f32_e32 v6, v4, v4
	v_and_b32_e32 v4, 0xffff0000, v147
	v_fmac_f32_e32 v6, v4, v4
	v_lshlrev_b32_e32 v4, 16, v148
	v_fmac_f32_e32 v6, v4, v4
	v_and_b32_e32 v4, 0xffff0000, v148
	v_fmac_f32_e32 v6, v4, v4
	v_lshlrev_b32_e32 v4, 16, v149
	v_fmac_f32_e32 v6, v4, v4
	v_and_b32_e32 v4, 0xffff0000, v149
	v_fmac_f32_e32 v6, v4, v4
	v_lshlrev_b32_e32 v4, 16, v150
	v_fmac_f32_e32 v6, v4, v4
	v_and_b32_e32 v4, 0xffff0000, v150
	v_fmac_f32_e32 v6, v4, v4
	v_lshlrev_b32_e32 v4, 16, v151
	v_fmac_f32_e32 v6, v4, v4
	v_and_b32_e32 v4, 0xffff0000, v151
	v_fmac_f32_e32 v6, v4, v4
	v_and_b32_e32 v5, 0xffff0000, v152
	v_lshlrev_b32_e32 v4, 16, v152
	v_pk_mul_f32 v[4:5], v[4:5], v[4:5]
	s_ashr_i32 s1, s0, 31
	v_add_f32_e32 v4, v4, v6
	v_add_f32_e32 v6, v5, v4
	v_and_b32_e32 v5, 0xffff0000, v153
	v_lshlrev_b32_e32 v4, 16, v153
	v_pk_mul_f32 v[4:5], v[4:5], v[4:5]
	s_lshl_b64 s[0:1], s[0:1], 2
	v_add_f32_e32 v4, v4, v6
	v_add_f32_e32 v6, v5, v4
	v_and_b32_e32 v5, 0xffff0000, v154
	v_lshlrev_b32_e32 v4, 16, v154
	v_pk_mul_f32 v[4:5], v[4:5], v[4:5]
	s_add_u32 s0, s21, s0
	v_add_f32_e32 v4, v4, v6
	v_add_f32_e32 v6, v5, v4
	v_and_b32_e32 v5, 0xffff0000, v155
	v_lshlrev_b32_e32 v4, 16, v155
	v_pk_mul_f32 v[4:5], v[4:5], v[4:5]
	s_addc_u32 s1, s22, s1
	v_add_f32_e32 v4, v4, v6
	s_ashr_i32 s3, s2, 31
	v_add_f32_e32 v4, v5, v4
	v_mov_b32_e32 v5, v157
	s_lshl_b64 s[0:1], s[2:3], 2
	s_add_u32 s0, s21, s0
	s_addc_u32 s1, s22, s1
	v_mov_b32_e32 v7, v166
	v_mov_b32_e32 v6, v4
	s_nop 1
	v_permlane32_swap_b32_e32 v4, v6
	s_mov_b32 s0, 0x45fd2000
	v_subrev_u32_e32 v223, s44, v8
	s_barrier
	v_mad_i32_i24 v8, v199, s23, v202
	v_add_u32_e32 v205, v216, v217
	s_mov_b64 s[2:3], exec
	v_lshl_add_u32 v8, s23, 7, v204
	s_waitcnt vmcnt(0)
	v_pk_add_f32 v[4:5], v[4:5], v[6:7]
	s_nop 0
	v_mul_f32_e32 v4, v4, v5
	v_cmp_gt_f32_e32 vcc, s0, v4
	s_nop 1
	s_cmp_eq_u64 vcc, s[2:3]
	s_cbranch_scc1 .Latt_flag_skip
	s_add_i32 s12, s15, 1
	v_mov_b32_e32 v178, 0x27f80
	v_mov_b32_e32 v179, s12
	ds_write_b32 v178, v179
